# guconv2: layer-0 down-proj weight conversion spread over the gate/up GEMM K loop (one 1 KB piece per K iteration and wave, counted waits 9/9/8/8, one 16-B store per unit in the epilogue); NA converts
# baseline (speedup 1.0000x reference)
.LBB0_684:
	v_lshrrev_b32_e32 v7, 1, v194
	s_add_u32 s46, s12, 0x3a000000
	v_and_b32_e32 v7, 24, v7
	s_addc_u32 s47, s13, 0
	v_and_b32_e32 v6, 15, v194
	v_lshlrev_b32_e32 v8, 1, v7
	s_add_u32 s48, s40, 0x80
	v_lshl_or_b32 v198, s4, 6, v6
	v_lshl_or_b32 v6, v6, 6, v8
	v_lshlrev_b32_e32 v8, 2, v194
	s_addc_u32 s49, s41, 0
	s_lshl_b32 s4, s4, 13
	v_and_b32_e32 v8, 32, v8
	v_bitop3_b32 v9, v6, s4, v8 bitop3:0xde
	s_lshl_b32 s4, s5, 5
	s_and_b32 s39, s4, 0x60
	s_lshl_b32 s4, s39, 7
	v_bitop3_b32 v6, v6, s4, v8 bitop3:0xde
	s_add_u32 s4, s58, 0x80
	s_waitcnt vmcnt(2)
	s_barrier
	s_addc_u32 s5, s59, 0
	s_add_i32 s76, s35, 0x18000
	s_mov_b32 s51, m0
	s_mov_b32 m0, s76
	s_nop 0
	global_load_lds_dwordx4 v196, s[4:5]
	s_mov_b32 m0, s51
	s_add_i32 s77, s35, 0x1a000
	s_mov_b32 s51, m0
	s_mov_b32 m0, s77
	s_nop 0
	global_load_lds_dwordx4 v197, s[4:5]
	s_mov_b32 m0, s51
	s_add_i32 s78, s35, 0x8000
	s_mov_b32 s4, m0
	s_mov_b32 m0, s78
	s_nop 0
	global_load_lds_dwordx4 v218, s[48:49]
	s_mov_b32 m0, s4
	s_add_i32 s79, s35, 0xa000
	s_mov_b32 s4, m0
	s_mov_b32 m0, s79
	s_nop 0
	global_load_lds_dwordx4 v215, s[48:49]
	s_mov_b32 m0, s4
	s_add_u32 s4, s58, 0x20080
	s_addc_u32 s5, s59, 0
	s_add_i32 s80, s35, 0x1c000
	s_mov_b32 s48, m0
	s_mov_b32 m0, s80
	s_nop 0
	global_load_lds_dwordx4 v196, s[4:5]
	s_mov_b32 m0, s48
	s_add_i32 s81, s35, 0x1e000
	s_mov_b32 s48, m0
	s_mov_b32 m0, s81
	s_nop 0
	global_load_lds_dwordx4 v197, s[4:5]
	s_mov_b32 m0, s48
	s_waitcnt vmcnt(6)
	s_add_i32 s82, s35, 0xc000
	s_cmpk_lt_u32 s17, 0x100
	v_mov_b32_e32 v67, 0
	s_cselect_b64 s[48:49], -1, 0
	v_or_b32_e32 v199, s39, v7
	v_readfirstlane_b32 s89, v0
	v_readfirstlane_b32 s90, v0
	v_mov_b32_e32 v200, s50
	v_mov_b32_e32 v210, s19
	s_mov_b32 s83, 0x20000
	s_mov_b64 s[50:51], 0x1000
	s_movk_i32 s84, 0x1000
	s_mov_b32 s54, 0x3d000000
	s_mov_b32 s85, 0xc0e00000
	s_mov_b32 s56, 0xc01d265f
	s_mov_b32 s86, 0x24000
	s_mov_b32 s87, 0x28000
	v_add_u32_e32 v201, 0, v6
	v_add_u32_e32 v202, 0, v9
	v_mov_b32_e32 v203, 0x40e00000
	v_mov_b32_e32 v66, 0
	v_mov_b32_e32 v68, v67
	v_mov_b32_e32 v69, v67
	v_mov_b32_e32 v70, 0
	v_mov_b32_e32 v71, v67
	v_mov_b32_e32 v72, v67
	v_mov_b32_e32 v73, v67
	v_mov_b32_e32 v74, 0
	v_mov_b32_e32 v75, v67
	v_mov_b32_e32 v76, v67
	v_mov_b32_e32 v77, v67
	v_mov_b32_e32 v78, 0
	v_mov_b32_e32 v79, v67
	v_mov_b32_e32 v80, v67
	v_mov_b32_e32 v81, v67
	v_mov_b32_e32 v82, 0
	v_mov_b32_e32 v83, v67
	v_mov_b32_e32 v84, v67
	v_mov_b32_e32 v85, v67
	v_mov_b32_e32 v86, 0
	v_mov_b32_e32 v87, v67
	v_mov_b32_e32 v88, v67
	v_mov_b32_e32 v89, v67
	v_mov_b32_e32 v90, 0
	v_mov_b32_e32 v91, v67
	v_mov_b32_e32 v92, v67
	v_mov_b32_e32 v93, v67
	v_mov_b32_e32 v94, 0
	v_mov_b32_e32 v95, v67
	v_mov_b32_e32 v96, v67
	v_mov_b32_e32 v97, v67
	v_mov_b32_e32 v98, 0
	v_mov_b32_e32 v99, v67
	v_mov_b32_e32 v100, v67
	v_mov_b32_e32 v101, v67
	v_mov_b32_e32 v102, 0
	v_mov_b32_e32 v103, v67
	v_mov_b32_e32 v104, v67
	v_mov_b32_e32 v105, v67
	v_mov_b32_e32 v106, 0
	v_mov_b32_e32 v107, v67
	v_mov_b32_e32 v108, v67
	v_mov_b32_e32 v109, v67
	v_mov_b32_e32 v110, 0
	v_mov_b32_e32 v111, v67
	v_mov_b32_e32 v112, v67
	v_mov_b32_e32 v113, v67
	v_mov_b32_e32 v114, 0
	v_mov_b32_e32 v115, v67
	v_mov_b32_e32 v116, v67
	v_mov_b32_e32 v117, v67
	v_mov_b32_e32 v118, 0
	v_mov_b32_e32 v119, v67
	v_mov_b32_e32 v120, v67
	v_mov_b32_e32 v121, v67
	v_mov_b32_e32 v122, 0
	v_mov_b32_e32 v123, v67
	v_mov_b32_e32 v124, v67
	v_mov_b32_e32 v125, v67
	v_mov_b32_e32 v126, 0
	v_mov_b32_e32 v127, v67
	v_mov_b32_e32 v128, v67
	v_mov_b32_e32 v129, v67
	s_waitcnt vmcnt(6)
	v_mov_b32_e32 v130, 0
	v_mov_b32_e32 v131, v67
	v_mov_b32_e32 v132, v67
	v_mov_b32_e32 v133, v67
	v_mov_b32_e32 v134, 0
	v_mov_b32_e32 v135, v67
	v_mov_b32_e32 v136, v67
	v_mov_b32_e32 v137, v67
	s_waitcnt vmcnt(4)
	v_mov_b32_e32 v138, 0
	v_mov_b32_e32 v139, v67
	v_mov_b32_e32 v140, v67
	v_mov_b32_e32 v141, v67
	v_mov_b32_e32 v142, 0
	v_mov_b32_e32 v143, v67
	v_mov_b32_e32 v144, v67
	v_mov_b32_e32 v145, v67
	s_waitcnt vmcnt(2)
	v_mov_b32_e32 v146, 0
	v_mov_b32_e32 v147, v67
	v_mov_b32_e32 v148, v67
	v_mov_b32_e32 v149, v67
	v_mov_b32_e32 v150, 0
	v_mov_b32_e32 v151, v67
	v_mov_b32_e32 v152, v67
	v_mov_b32_e32 v153, v67
	s_waitcnt vmcnt(0)
	v_mov_b32_e32 v154, 0
	v_mov_b32_e32 v155, v67
	v_mov_b32_e32 v156, v67
	v_mov_b32_e32 v157, v67
	v_mov_b32_e32 v158, 0
	v_mov_b32_e32 v159, v67
	v_mov_b32_e32 v160, v67
	v_mov_b32_e32 v161, v67
	v_mov_b32_e32 v162, 0
	v_mov_b32_e32 v163, v67
	v_mov_b32_e32 v164, v67
	v_mov_b32_e32 v165, v67
	v_mov_b32_e32 v166, 0
	v_mov_b32_e32 v167, v67
	v_mov_b32_e32 v168, v67
	v_mov_b32_e32 v169, v67
	v_mov_b32_e32 v170, 0
	v_mov_b32_e32 v171, v67
	v_mov_b32_e32 v172, v67
	v_mov_b32_e32 v173, v67
	v_mov_b32_e32 v174, 0
	v_mov_b32_e32 v175, v67
	v_mov_b32_e32 v176, v67
	v_mov_b32_e32 v177, v67
	v_mov_b32_e32 v178, 0
	v_mov_b32_e32 v179, v67
	v_mov_b32_e32 v180, v67
	v_mov_b32_e32 v181, v67
	v_mov_b32_e32 v182, 0
	v_mov_b32_e32 v183, v67
	v_mov_b32_e32 v184, v67
	v_mov_b32_e32 v185, v67
	v_mov_b32_e32 v186, 0
	v_mov_b32_e32 v187, v67
	v_mov_b32_e32 v188, v67
	v_mov_b32_e32 v189, v67
	v_mov_b32_e32 v190, 0
	v_mov_b32_e32 v191, v67
	v_mov_b32_e32 v192, v67
	v_mov_b32_e32 v193, v67
	s_barrier
	s_load_dwordx2 s[100:101], s[0:1], 0xc0
	v_readfirstlane_b32 s98, v0
	s_lshr_b32 s98, s98, 6
	s_lshl_b32 s99, s2, 3
	s_add_i32 s98, s98, s99
	s_and_b32 s98, s98, 0x7ff
	v_and_b32_e32 v240, 63, v0
	v_lshrrev_b32_e32 v241, 4, v240
	v_and_b32_e32 v240, 15, v240
	v_lshlrev_b32_e32 v242, 4, v240
	v_lshl_add_u32 v242, v241, 12, v242
	v_lshl_add_u32 v243, v240, 2, v241
	v_lshlrev_b32_e32 v243, 10, v243
	s_lshl_b32 s99, s98, 16
	v_add_u32_e32 v250, s99, v242
	v_mov_b32_e32 v251, 0
	s_waitcnt lgkmcnt(0)
	v_lshl_add_u64 v[250:251], v[250:251], 0, s[100:101]
	s_load_dwordx2 s[100:101], s[0:1], 0xd8
	s_lshr_b32 s99, s98, 6
	s_lshl_b32 s99, s99, 20
	s_and_b32 s98, s98, 63
	s_lshl_b32 s98, s98, 4
	s_add_i32 s99, s99, s98
	s_add_i32 s99, s99, 0x11800000
	v_add_u32_e32 v252, s99, v243
	v_mov_b32_e32 v253, 0
	s_waitcnt lgkmcnt(0)
	v_lshl_add_u64 v[252:253], v[252:253], 0, s[100:101]
	s_mov_b32 s98, 0
	s_branch .LBB0_687

.LBB0_689:
	s_cmp_lg_u32 s39, 4
	s_cselect_b64 s[70:71], -1, 0
	s_add_u32 s4, s58, s64
	v_add_u32_e32 v2, 0x10000, v201
	v_add_u32_e32 v14, 0x14000, v201
	s_addc_u32 s5, s59, s65
	ds_read_b128 v[18:21], v2
	ds_read_b128 v[22:25], v2 offset:1024
	ds_read_b128 v[26:29], v2 offset:2048
	ds_read_b128 v[30:33], v2 offset:3072
	ds_read_b128 v[2:5], v14
	ds_read_b128 v[6:9], v14 offset:1024
	ds_read_b128 v[10:13], v14 offset:2048
	ds_read_b128 v[14:17], v14 offset:3072
	s_add_u32 s4, s4, 0xa3100100
	s_addc_u32 s5, s5, -1
	s_cmp_eq_u32 s39, 4
	s_cselect_b64 s[68:69], -1, 0
	s_and_b64 vcc, s[68:69], exec
	s_cselect_b32 s67, s17, s5
	s_cselect_b32 s66, s19, s4
	ds_read_b128 v[34:37], v202
	ds_read_b128 v[38:41], v202 offset:1024
	ds_read_b128 v[42:45], v202 offset:2048
	ds_read_b128 v[46:49], v202 offset:3072
	ds_read_b128 v[50:53], v202 offset:4096
	ds_read_b128 v[54:57], v202 offset:5120
	ds_read_b128 v[58:61], v202 offset:6144
	ds_read_b128 v[62:65], v202 offset:7168
	s_add_u32 s4, s12, s64
	s_addc_u32 s5, s13, s65
	s_add_u32 s4, s4, 0x80
	s_addc_u32 s5, s5, 0
	s_mov_b32 s91, m0
	s_mov_b32 m0, s82
	s_nop 0
	global_load_lds_dwordx4 v216, s[4:5]
	s_mov_b32 m0, s91
	s_add_i32 s91, s35, 0xe000
	s_mov_b32 s92, m0
	s_mov_b32 m0, s91
	s_nop 0
	global_load_lds_dwordx4 v217, s[4:5]
	s_mov_b32 m0, s92
	s_add_i32 s100, s39, 2
	s_lshl_b32 s100, s100, 13
	s_and_b32 s101, s98, 15
	s_lshl_b32 s101, s101, 8
	s_add_u32 s100, s100, s101
	s_mov_b32 s101, 0
	v_lshl_add_u64 v[240:241], v[250:251], 0, s[100:101]
	global_load_dwordx4 v[224:227], v[240:241], off
	s_waitcnt vmcnt(9)
	s_waitcnt lgkmcnt(0)
	s_barrier
	s_setprio 1
	s_waitcnt lgkmcnt(0)
	v_mfma_f32_16x16x128_f8f6f4 v[190:193], v[18:25], v[34:41], v[190:193]
	v_mfma_f32_16x16x128_f8f6f4 v[186:189], v[26:33], v[34:41], v[186:189]
	v_mfma_f32_16x16x128_f8f6f4 v[182:185], v[18:25], v[42:49], v[182:185]
	v_mfma_f32_16x16x128_f8f6f4 v[178:181], v[26:33], v[42:49], v[178:181]
	v_mfma_f32_16x16x128_f8f6f4 v[174:177], v[18:25], v[50:57], v[174:177]
	v_mfma_f32_16x16x128_f8f6f4 v[170:173], v[26:33], v[50:57], v[170:173]
	v_mfma_f32_16x16x128_f8f6f4 v[166:169], v[18:25], v[58:65], v[166:169]
	v_mfma_f32_16x16x128_f8f6f4 v[162:165], v[26:33], v[58:65], v[162:165]
	s_setprio 0
	s_setprio 1
	v_mfma_f32_16x16x128_f8f6f4 v[158:161], v[2:9], v[34:41], v[158:161]
	v_mfma_f32_16x16x128_f8f6f4 v[154:157], v[10:17], v[34:41], v[154:157]
	v_mfma_f32_16x16x128_f8f6f4 v[150:153], v[2:9], v[42:49], v[150:153]
	v_mfma_f32_16x16x128_f8f6f4 v[146:149], v[10:17], v[42:49], v[146:149]
	v_mfma_f32_16x16x128_f8f6f4 v[142:145], v[2:9], v[50:57], v[142:145]
	v_mfma_f32_16x16x128_f8f6f4 v[138:141], v[10:17], v[50:57], v[138:141]
	v_mfma_f32_16x16x128_f8f6f4 v[134:137], v[2:9], v[58:65], v[134:137]
	v_mfma_f32_16x16x128_f8f6f4 v[130:133], v[10:17], v[58:65], v[130:133]
	s_setprio 0
	s_barrier
	ds_read_b128 v[58:61], v202 offset:16384
	ds_read_b128 v[62:65], v202 offset:17408
	ds_read_b128 v[50:53], v202 offset:18432
	ds_read_b128 v[54:57], v202 offset:19456
	ds_read_b128 v[42:45], v202 offset:20480
	ds_read_b128 v[46:49], v202 offset:21504
	ds_read_b128 v[34:37], v202 offset:22528
	ds_read_b128 v[38:41], v202 offset:23552
	s_mov_b32 s4, m0
	s_mov_b32 m0, s53
	s_nop 0
	global_load_lds_dwordx4 v196, s[66:67]
	s_mov_b32 m0, s4
	s_nop 0
	s_mov_b32 s4, m0
	s_mov_b32 m0, s55
	s_nop 0
	global_load_lds_dwordx4 v197, s[66:67]
	s_mov_b32 m0, s4
	s_add_u32 s4, s66, 0x20000
	s_addc_u32 s5, s67, 0
	s_mov_b32 s91, m0
	s_mov_b32 m0, s57
	s_nop 0
	global_load_lds_dwordx4 v196, s[4:5]
	s_mov_b32 m0, s91
	s_nop 0
	s_mov_b32 s91, m0
	s_mov_b32 m0, s72
	s_nop 0
	global_load_lds_dwordx4 v197, s[4:5]
	s_mov_b32 m0, s91
	s_mov_b64 s[4:5], -1
	s_cbranch_vccnz .LBB0_691
	s_add_u32 s4, s40, s64
	s_addc_u32 s5, s41, s65
	s_add_u32 s4, s4, 0xa3100100
	s_addc_u32 s5, s5, -1
	s_mov_b32 s91, m0
	s_mov_b32 m0, s35
	s_nop 0
	global_load_lds_dwordx4 v218, s[4:5]
	s_mov_b32 m0, s91
	s_nop 0
	s_mov_b32 s91, m0
	s_mov_b32 m0, s73
	s_nop 0
	global_load_lds_dwordx4 v215, s[4:5]
	s_mov_b32 m0, s91
	s_mov_b64 s[4:5], 0

.LBB0_693:
	s_waitcnt vmcnt(9)
	s_waitcnt lgkmcnt(0)
	s_barrier
	s_setprio 1
	s_waitcnt lgkmcnt(6)
	v_mfma_f32_16x16x128_f8f6f4 v[126:129], v[18:25], v[58:65], v[126:129]
	v_mfma_f32_16x16x128_f8f6f4 v[122:125], v[26:33], v[58:65], v[122:125]
	s_waitcnt lgkmcnt(4)
	v_mfma_f32_16x16x128_f8f6f4 v[118:121], v[18:25], v[50:57], v[118:121]
	v_mfma_f32_16x16x128_f8f6f4 v[114:117], v[26:33], v[50:57], v[114:117]
	s_waitcnt lgkmcnt(2)
	v_mfma_f32_16x16x128_f8f6f4 v[110:113], v[18:25], v[42:49], v[110:113]
	v_mfma_f32_16x16x128_f8f6f4 v[106:109], v[26:33], v[42:49], v[106:109]
	s_waitcnt lgkmcnt(0)
	v_mfma_f32_16x16x128_f8f6f4 v[102:105], v[18:25], v[34:41], v[102:105]
	v_mfma_f32_16x16x128_f8f6f4 v[98:101], v[26:33], v[34:41], v[98:101]
	s_setprio 0
	s_setprio 1
	v_mfma_f32_16x16x128_f8f6f4 v[94:97], v[2:9], v[58:65], v[94:97]
	v_mfma_f32_16x16x128_f8f6f4 v[90:93], v[10:17], v[58:65], v[90:93]
	v_mfma_f32_16x16x128_f8f6f4 v[86:89], v[2:9], v[50:57], v[86:89]
	v_mfma_f32_16x16x128_f8f6f4 v[82:85], v[10:17], v[50:57], v[82:85]
	v_mfma_f32_16x16x128_f8f6f4 v[78:81], v[2:9], v[42:49], v[78:81]
	v_mfma_f32_16x16x128_f8f6f4 v[74:77], v[10:17], v[42:49], v[74:77]
	v_mfma_f32_16x16x128_f8f6f4 v[70:73], v[2:9], v[34:41], v[70:73]
	v_mfma_f32_16x16x128_f8f6f4 v[66:69], v[10:17], v[34:41], v[66:69]
	s_setprio 0
	s_barrier
	v_add_u32_e32 v2, 0x18000, v201
	v_add_u32_e32 v14, 0x1c000, v201
	ds_read_b128 v[18:21], v2
	ds_read_b128 v[22:25], v2 offset:1024
	ds_read_b128 v[26:29], v2 offset:2048
	ds_read_b128 v[30:33], v2 offset:3072
	ds_read_b128 v[2:5], v14
	ds_read_b128 v[6:9], v14 offset:1024
	ds_read_b128 v[10:13], v14 offset:2048
	ds_read_b128 v[14:17], v14 offset:3072
	ds_read_b128 v[58:61], v202 offset:32768
	ds_read_b128 v[62:65], v202 offset:33792
	ds_read_b128 v[50:53], v202 offset:34816
	ds_read_b128 v[54:57], v202 offset:35840
	ds_read_b128 v[42:45], v202 offset:36864
	ds_read_b128 v[46:49], v202 offset:37888
	ds_read_b128 v[34:37], v202 offset:38912
	ds_read_b128 v[38:41], v202 offset:39936
	v_cndmask_b32_e64 v219, 0, 1, s[70:71]
	v_cmp_ne_u32_e64 s[4:5], 1, v219
	s_andn2_b64 vcc, exec, s[70:71]
	s_mov_b64 s[70:71], -1
	s_cbranch_vccnz .LBB0_695
	s_add_u32 s70, s40, s64
	s_addc_u32 s71, s41, s65
	s_add_u32 s70, s70, 0xa3100100
	s_addc_u32 s71, s71, -1
	s_mov_b32 s91, m0
	s_mov_b32 m0, s74
	s_nop 0
	global_load_lds_dwordx4 v216, s[70:71]
	s_mov_b32 m0, s91
	s_nop 0
	s_mov_b32 s91, m0
	s_mov_b32 m0, s75
	s_nop 0
	global_load_lds_dwordx4 v217, s[70:71]
	s_mov_b32 m0, s91
	s_mov_b64 s[70:71], 0

.LBB0_697:
	s_waitcnt vmcnt(8)
	v_mul_f32_e32 v224, 0x42000000, v224
	v_mul_f32_e32 v225, 0x42000000, v225
	v_mul_f32_e32 v226, 0x42000000, v226
	v_mul_f32_e32 v227, 0x42000000, v227
	v_mov_b32_e32 v244, v245
	v_mov_b32_e32 v245, v246
	v_permlane32_swap_b32_e32 v224, v226
	v_permlane32_swap_b32_e32 v225, v227
	v_mov_b32_e32 v246, v247
	s_nop 0
	v_permlane16_swap_b32_e32 v224, v225
	v_permlane16_swap_b32_e32 v226, v227
	s_nop 1
	v_cvt_pk_fp8_f32 v247, v224, v225
	v_cvt_pk_fp8_f32 v247, v226, v227 op_sel:[0,0,1]
	s_add_i32 s70, s64, 0xa3100180
	s_waitcnt lgkmcnt(0)
	s_and_b64 s[68:69], s[68:69], exec
	s_cselect_b32 s70, 0x80, s70
	s_add_u32 s68, s66, 0x80
	s_addc_u32 s69, s67, 0
	s_barrier
	s_setprio 1
	s_waitcnt lgkmcnt(6)
	v_mfma_f32_16x16x128_f8f6f4 v[190:193], v[18:25], v[58:65], v[190:193]
	v_mfma_f32_16x16x128_f8f6f4 v[186:189], v[26:33], v[58:65], v[186:189]
	s_waitcnt lgkmcnt(4)
	v_mfma_f32_16x16x128_f8f6f4 v[182:185], v[18:25], v[50:57], v[182:185]
	v_mfma_f32_16x16x128_f8f6f4 v[178:181], v[26:33], v[50:57], v[178:181]
	s_waitcnt lgkmcnt(2)
	v_mfma_f32_16x16x128_f8f6f4 v[174:177], v[18:25], v[42:49], v[174:177]
	v_mfma_f32_16x16x128_f8f6f4 v[170:173], v[26:33], v[42:49], v[170:173]
	s_waitcnt lgkmcnt(0)
	v_mfma_f32_16x16x128_f8f6f4 v[166:169], v[18:25], v[34:41], v[166:169]
	v_mfma_f32_16x16x128_f8f6f4 v[162:165], v[26:33], v[34:41], v[162:165]
	s_setprio 0
	s_setprio 1
	v_mfma_f32_16x16x128_f8f6f4 v[158:161], v[2:9], v[58:65], v[158:161]
	v_mfma_f32_16x16x128_f8f6f4 v[154:157], v[10:17], v[58:65], v[154:157]
	v_mfma_f32_16x16x128_f8f6f4 v[150:153], v[2:9], v[50:57], v[150:153]
	v_mfma_f32_16x16x128_f8f6f4 v[146:149], v[10:17], v[50:57], v[146:149]
	v_mfma_f32_16x16x128_f8f6f4 v[142:145], v[2:9], v[42:49], v[142:145]
	v_mfma_f32_16x16x128_f8f6f4 v[138:141], v[10:17], v[42:49], v[138:141]
	v_mfma_f32_16x16x128_f8f6f4 v[134:137], v[2:9], v[34:41], v[134:137]
	v_mfma_f32_16x16x128_f8f6f4 v[130:133], v[10:17], v[34:41], v[130:133]
	s_setprio 0
	s_barrier
	ds_read_b128 v[58:61], v202 offset:49152
	ds_read_b128 v[62:65], v202 offset:50176
	ds_read_b128 v[50:53], v202 offset:51200
	ds_read_b128 v[54:57], v202 offset:52224
	ds_read_b128 v[42:45], v202 offset:53248
	ds_read_b128 v[46:49], v202 offset:54272
	ds_read_b128 v[34:37], v202 offset:55296
	ds_read_b128 v[38:41], v202 offset:56320
	s_mov_b32 s71, m0
	s_mov_b32 m0, s76
	s_nop 0
	global_load_lds_dwordx4 v196, s[68:69]
	s_mov_b32 m0, s71
	s_add_u32 s66, s66, 0x20080
	s_mov_b32 s71, m0
	s_mov_b32 m0, s77
	s_nop 0
	global_load_lds_dwordx4 v197, s[68:69]
	s_mov_b32 m0, s71
	s_addc_u32 s67, s67, 0
	s_mov_b32 s68, m0
	s_mov_b32 m0, s80
	s_nop 0
	global_load_lds_dwordx4 v196, s[66:67]
	s_mov_b32 m0, s68
	s_nop 0
	s_mov_b32 s68, m0
	s_mov_b32 m0, s81
	s_nop 0
	global_load_lds_dwordx4 v197, s[66:67]
	s_mov_b32 m0, s68
	s_add_u32 s66, s40, s70
	s_addc_u32 s67, s41, 0
	s_and_b64 vcc, exec, s[4:5]
	s_mov_b64 s[4:5], -1
	s_cbranch_vccnz .LBB0_699
	s_mov_b32 s4, m0
	s_mov_b32 m0, s78
	s_nop 0
	global_load_lds_dwordx4 v218, s[66:67]
	s_mov_b32 m0, s4
	s_nop 0
	s_mov_b32 s4, m0
	s_mov_b32 m0, s79
	s_nop 0
	global_load_lds_dwordx4 v215, s[66:67]
	s_mov_b32 m0, s4
	s_mov_b64 s[4:5], 0

.LBB0_716:
	s_ashr_i32 s39, s38, 31
	s_lshl_b64 s[66:67], s[38:39], 13
	v_lshl_or_b32 v20, s28, 7, v199
	s_add_u32 s66, s20, s66
	s_addc_u32 s67, s21, s67
	v_ashrrev_i32_e32 v21, 31, v20
	v_lshl_add_u64 v[6:7], v[20:21], 2, s[66:67]
	global_load_dwordx4 v[14:17], v[6:7], off
	global_load_dwordx4 v[10:13], v[6:7], off offset:16
	v_add_co_u32_e32 v2, vcc, s84, v6
	v_mov_b32_e32 v25, 0
	s_nop 0
	v_addc_co_u32_e32 v3, vcc, 0, v7, vcc
	v_lshl_add_u64 v[6:7], v[6:7], 0, s[50:51]
	global_load_dwordx4 v[2:5], v[2:3], off
	v_mov_b32_e32 v24, 0
	global_load_dwordx4 v[6:9], v[6:7], off offset:16
	v_lshl_add_u32 v22, v210, 8, v198
	v_ashrrev_i32_e32 v23, 31, v22
	v_lshlrev_b64 v[18:19], 10, v[22:23]
	v_lshl_add_u64 v[18:19], s[46:47], 0, v[18:19]
	v_lshl_add_u64 v[18:19], v[18:19], 0, v[20:21]
	v_or_b32_e32 v26, 16, v22
	v_ashrrev_i32_e32 v27, 31, v26
	s_waitcnt vmcnt(3)
	v_pk_fma_f32 v[30:31], v[190:191], s[54:55], v[14:15] op_sel_hi:[1,0,1]
	s_waitcnt vmcnt(2)
	v_pk_fma_f32 v[34:35], v[186:187], s[54:55], v[10:11] op_sel_hi:[1,0,1]
	v_pk_fma_f32 v[32:33], v[188:189], s[54:55], v[12:13] op_sel_hi:[1,0,1]
	v_min_f32_e32 v34, 0x40e00000, v34
	v_min_f32_e32 v35, 0x40e00000, v35
	v_pk_mul_f32 v[56:57], v[34:35], s[56:57] op_sel_hi:[1,0]
	v_min_f32_e32 v30, 0x40e00000, v30
	v_exp_f32_e32 v56, v56
	v_exp_f32_e32 v57, v57
	v_min_f32_e32 v31, 0x40e00000, v31
	v_min_f32_e32 v32, 0x40e00000, v32
	v_min_f32_e32 v33, 0x40e00000, v33
	v_pk_mul_f32 v[52:53], v[30:31], s[56:57] op_sel_hi:[1,0]
	v_pk_mul_f32 v[58:59], v[32:33], s[56:57] op_sel_hi:[1,0]
	v_exp_f32_e32 v52, v52
	v_exp_f32_e32 v53, v53
	v_exp_f32_e32 v58, v58
	v_exp_f32_e32 v59, v59
	v_pk_add_f32 v[56:57], v[56:57], 1.0 op_sel_hi:[1,0]
	v_pk_fma_f32 v[28:29], v[192:193], s[54:55], v[16:17] op_sel_hi:[1,0,1]
	v_rcp_f32_e32 v56, v56
	v_rcp_f32_e32 v57, v57
	v_min_f32_e32 v28, 0x40e00000, v28
	v_min_f32_e32 v29, 0x40e00000, v29
	s_waitcnt vmcnt(0)
	s_and_b32 s100, s98, 15
	s_lshl_b32 s100, s100, 16
	s_mov_b32 s101, 0
	v_lshl_add_u64 v[240:241], v[252:253], 0, s[100:101]
	global_store_dwordx4 v[240:241], v[244:247], off
	s_add_i32 s98, s98, 1
	v_pk_fma_f32 v[50:51], v[154:155], s[54:55], v[6:7] op_sel_hi:[1,0,1]
	v_pk_mul_f32 v[54:55], v[28:29], s[56:57] op_sel_hi:[1,0]
	v_pk_add_f32 v[52:53], v[52:53], 1.0 op_sel_hi:[1,0]
	v_exp_f32_e32 v54, v54
	v_exp_f32_e32 v55, v55
	v_med3_f32 v50, v50, s85, v203
	v_med3_f32 v51, v51, s85, v203
	v_pk_add_f32 v[58:59], v[58:59], 1.0 op_sel_hi:[1,0]
	v_rcp_f32_e32 v52, v52
	v_rcp_f32_e32 v53, v53
	v_pk_add_f32 v[50:51], v[50:51], 1.0 op_sel_hi:[1,0]
	v_rcp_f32_e32 v58, v58
	v_rcp_f32_e32 v59, v59
	v_pk_mul_f32 v[34:35], v[34:35], v[56:57]
	v_pk_fma_f32 v[46:47], v[158:159], s[54:55], v[2:3] op_sel_hi:[1,0,1]
	v_pk_mul_f32 v[34:35], v[50:51], v[34:35]
	v_pk_fma_f32 v[48:49], v[156:157], s[54:55], v[8:9] op_sel_hi:[1,0,1]
	v_med3_f32 v46, v46, s85, v203
	v_med3_f32 v47, v47, s85, v203
	v_cvt_pk_fp8_f32 v25, v34, v35
	v_pk_fma_f32 v[38:39], v[182:183], s[54:55], v[14:15] op_sel_hi:[1,0,1]
	v_med3_f32 v48, v48, s85, v203
	v_med3_f32 v49, v49, s85, v203
	v_pk_add_f32 v[46:47], v[46:47], 1.0 op_sel_hi:[1,0]
	v_pk_add_f32 v[54:55], v[54:55], 1.0 op_sel_hi:[1,0]
	v_pk_mul_f32 v[30:31], v[30:31], v[52:53]
	v_min_f32_e32 v38, 0x40e00000, v38
	v_min_f32_e32 v39, 0x40e00000, v39
	v_pk_add_f32 v[48:49], v[48:49], 1.0 op_sel_hi:[1,0]
	v_rcp_f32_e32 v54, v54
	v_rcp_f32_e32 v55, v55
	v_pk_mul_f32 v[32:33], v[32:33], v[58:59]
	v_pk_mul_f32 v[30:31], v[46:47], v[30:31]
	v_pk_fma_f32 v[36:37], v[184:185], s[54:55], v[16:17] op_sel_hi:[1,0,1]
	v_pk_mul_f32 v[218:219], v[38:39], s[56:57] op_sel_hi:[1,0]
	v_cvt_pk_fp8_f32 v24, v30, v31
	v_pk_mul_f32 v[30:31], v[48:49], v[32:33]
	v_pk_fma_f32 v[44:45], v[160:161], s[54:55], v[4:5] op_sel_hi:[1,0,1]
	v_exp_f32_e32 v218, v218
	v_exp_f32_e32 v219, v219
	v_cvt_pk_fp8_f32 v25, v30, v31 op_sel:[0,0,1]
	v_min_f32_e32 v30, 0x40e00000, v36
	v_min_f32_e32 v31, 0x40e00000, v37
	v_med3_f32 v44, v44, s85, v203
	v_med3_f32 v45, v45, s85, v203
	v_pk_mul_f32 v[32:33], v[30:31], s[56:57] op_sel_hi:[1,0]
	v_pk_add_f32 v[44:45], v[44:45], 1.0 op_sel_hi:[1,0]
	v_pk_mul_f32 v[28:29], v[28:29], v[54:55]
	v_exp_f32_e32 v32, v32
	v_exp_f32_e32 v33, v33
	v_pk_mul_f32 v[28:29], v[44:45], v[28:29]
	v_pk_fma_f32 v[42:43], v[178:179], s[54:55], v[10:11] op_sel_hi:[1,0,1]
	v_cvt_pk_fp8_f32 v24, v28, v29 op_sel:[0,0,1]
	v_pk_add_f32 v[28:29], v[218:219], 1.0 op_sel_hi:[1,0]
	v_pk_add_f32 v[32:33], v[32:33], 1.0 op_sel_hi:[1,0]
	v_rcp_f32_e32 v28, v28
	v_rcp_f32_e32 v29, v29
	v_min_f32_e32 v34, 0x40e00000, v42
	v_min_f32_e32 v35, 0x40e00000, v43
	v_pk_fma_f32 v[62:63], v[150:151], s[54:55], v[2:3] op_sel_hi:[1,0,1]
	v_rcp_f32_e32 v32, v32
	v_rcp_f32_e32 v33, v33
	v_pk_mul_f32 v[36:37], v[34:35], s[56:57] op_sel_hi:[1,0]
	v_med3_f32 v62, v62, s85, v203
	v_med3_f32 v63, v63, s85, v203
	v_exp_f32_e32 v36, v36
	v_exp_f32_e32 v37, v37
	v_pk_fma_f32 v[60:61], v[152:153], s[54:55], v[4:5] op_sel_hi:[1,0,1]
	global_store_dwordx2 v[18:19], v[24:25], off
	v_pk_add_f32 v[24:25], v[62:63], 1.0 op_sel_hi:[1,0]
	v_pk_mul_f32 v[28:29], v[38:39], v[28:29]
	v_pk_mul_f32 v[30:31], v[30:31], v[32:33]
	v_pk_mul_f32 v[24:25], v[24:25], v[28:29]
	v_med3_f32 v28, v60, s85, v203
	v_med3_f32 v29, v61, s85, v203
	v_pk_add_f32 v[28:29], v[28:29], 1.0 op_sel_hi:[1,0]
	v_pk_fma_f32 v[40:41], v[180:181], s[54:55], v[12:13] op_sel_hi:[1,0,1]
	v_pk_mul_f32 v[28:29], v[28:29], v[30:31]
	v_pk_add_f32 v[30:31], v[36:37], 1.0 op_sel_hi:[1,0]
	v_mov_b32_e32 v38, 0
	v_rcp_f32_e32 v30, v30
	v_rcp_f32_e32 v31, v31
	v_cvt_pk_fp8_f32 v38, v24, v25
	v_pk_fma_f32 v[216:217], v[146:147], s[54:55], v[6:7] op_sel_hi:[1,0,1]
	v_mov_b32_e32 v39, 0
	v_pk_mul_f32 v[30:31], v[34:35], v[30:31]
	v_min_f32_e32 v34, 0x40e00000, v40
	v_min_f32_e32 v35, 0x40e00000, v41
	v_pk_mul_f32 v[36:37], v[34:35], s[56:57] op_sel_hi:[1,0]
	v_cvt_pk_fp8_f32 v38, v28, v29 op_sel:[0,0,1]
	v_exp_f32_e32 v36, v36
	v_exp_f32_e32 v37, v37
	v_pk_fma_f32 v[28:29], v[174:175], s[54:55], v[14:15] op_sel_hi:[1,0,1]
	v_med3_f32 v32, v216, s85, v203
	v_min_f32_e32 v28, 0x40e00000, v28
	v_pk_add_f32 v[36:37], v[36:37], 1.0 op_sel_hi:[1,0]
	v_min_f32_e32 v29, 0x40e00000, v29
	v_rcp_f32_e32 v36, v36
	v_rcp_f32_e32 v37, v37
	v_med3_f32 v33, v217, s85, v203
	v_pk_add_f32 v[32:33], v[32:33], 1.0 op_sel_hi:[1,0]
	v_pk_fma_f32 v[64:65], v[148:149], s[54:55], v[8:9] op_sel_hi:[1,0,1]
	v_pk_mul_f32 v[24:25], v[34:35], v[36:37]
	v_pk_mul_f32 v[36:37], v[28:29], s[56:57] op_sel_hi:[1,0]
	v_pk_mul_f32 v[30:31], v[32:33], v[30:31]
	v_exp_f32_e32 v36, v36
	v_exp_f32_e32 v37, v37
	v_cvt_pk_fp8_f32 v39, v30, v31
	v_med3_f32 v32, v64, s85, v203
	v_med3_f32 v33, v65, s85, v203
	v_pk_add_f32 v[36:37], v[36:37], 1.0 op_sel_hi:[1,0]
	v_pk_add_f32 v[32:33], v[32:33], 1.0 op_sel_hi:[1,0]
	v_rcp_f32_e32 v36, v36
	v_rcp_f32_e32 v37, v37
	v_pk_mul_f32 v[24:25], v[32:33], v[24:25]
	v_pk_fma_f32 v[32:33], v[170:171], s[54:55], v[10:11] op_sel_hi:[1,0,1]
	v_cvt_pk_fp8_f32 v39, v24, v25 op_sel:[0,0,1]
	v_lshlrev_b64 v[24:25], 10, v[26:27]
	v_pk_fma_f32 v[26:27], v[176:177], s[54:55], v[16:17] op_sel_hi:[1,0,1]
	v_pk_mul_f32 v[28:29], v[28:29], v[36:37]
	v_min_f32_e32 v26, 0x40e00000, v26
	v_min_f32_e32 v27, 0x40e00000, v27
	v_pk_mul_f32 v[36:37], v[26:27], s[56:57] op_sel_hi:[1,0]
	v_lshl_add_u64 v[24:25], s[46:47], 0, v[24:25]
	v_exp_f32_e32 v36, v36
	v_exp_f32_e32 v37, v37
	v_lshl_add_u64 v[24:25], v[24:25], 0, v[20:21]
	global_store_dwordx2 v[24:25], v[38:39], off
	v_pk_fma_f32 v[38:39], v[142:143], s[54:55], v[2:3] op_sel_hi:[1,0,1]
	v_pk_add_f32 v[36:37], v[36:37], 1.0 op_sel_hi:[1,0]
	v_med3_f32 v38, v38, s85, v203
	v_med3_f32 v39, v39, s85, v203
	v_pk_add_f32 v[38:39], v[38:39], 1.0 op_sel_hi:[1,0]
	v_min_f32_e32 v32, 0x40e00000, v32
	v_min_f32_e32 v33, 0x40e00000, v33
	v_pk_mul_f32 v[28:29], v[38:39], v[28:29]
	v_rcp_f32_e32 v36, v36
	v_rcp_f32_e32 v37, v37
	v_pk_mul_f32 v[38:39], v[32:33], s[56:57] op_sel_hi:[1,0]
	v_pk_fma_f32 v[34:35], v[144:145], s[54:55], v[4:5] op_sel_hi:[1,0,1]
	v_exp_f32_e32 v38, v38
	v_exp_f32_e32 v39, v39
	v_med3_f32 v34, v34, s85, v203
	v_med3_f32 v35, v35, s85, v203
	v_pk_add_f32 v[34:35], v[34:35], 1.0 op_sel_hi:[1,0]
	v_pk_mul_f32 v[26:27], v[26:27], v[36:37]
	v_pk_fma_f32 v[30:31], v[172:173], s[54:55], v[12:13] op_sel_hi:[1,0,1]
	v_pk_mul_f32 v[26:27], v[34:35], v[26:27]
	v_pk_add_f32 v[34:35], v[38:39], 1.0 op_sel_hi:[1,0]
	v_min_f32_e32 v30, 0x40e00000, v30
	v_rcp_f32_e32 v34, v34
	v_rcp_f32_e32 v35, v35
	v_min_f32_e32 v31, 0x40e00000, v31
	v_mov_b32_e32 v38, 0
	v_cvt_pk_fp8_f32 v38, v28, v29
	v_pk_mul_f32 v[32:33], v[32:33], v[34:35]
	v_pk_mul_f32 v[34:35], v[30:31], s[56:57] op_sel_hi:[1,0]
	v_pk_fma_f32 v[42:43], v[138:139], s[54:55], v[6:7] op_sel_hi:[1,0,1]
	v_exp_f32_e32 v34, v34
	v_exp_f32_e32 v35, v35
	v_med3_f32 v36, v42, s85, v203
	v_med3_f32 v37, v43, s85, v203
	v_pk_add_f32 v[36:37], v[36:37], 1.0 op_sel_hi:[1,0]
	v_pk_add_f32 v[34:35], v[34:35], 1.0 op_sel_hi:[1,0]
	v_cvt_pk_fp8_f32 v38, v26, v27 op_sel:[0,0,1]
	v_rcp_f32_e32 v34, v34
	v_rcp_f32_e32 v35, v35
	v_pk_fma_f32 v[26:27], v[166:167], s[54:55], v[14:15] op_sel_hi:[1,0,1]
	v_pk_mul_f32 v[32:33], v[36:37], v[32:33]
	v_mov_b32_e32 v39, 0
	v_min_f32_e32 v26, 0x40e00000, v26
	v_min_f32_e32 v27, 0x40e00000, v27
	v_pk_fma_f32 v[40:41], v[140:141], s[54:55], v[8:9] op_sel_hi:[1,0,1]
	v_cvt_pk_fp8_f32 v39, v32, v33
	v_pk_mul_f32 v[28:29], v[30:31], v[34:35]
	v_pk_mul_f32 v[34:35], v[26:27], s[56:57] op_sel_hi:[1,0]
	v_med3_f32 v36, v40, s85, v203
	v_med3_f32 v37, v41, s85, v203
	v_exp_f32_e32 v34, v34
	v_exp_f32_e32 v35, v35
	v_pk_add_f32 v[36:37], v[36:37], 1.0 op_sel_hi:[1,0]
	v_or_b32_e32 v24, 32, v22
	v_pk_mul_f32 v[28:29], v[36:37], v[28:29]
	v_ashrrev_i32_e32 v25, 31, v24
	v_cvt_pk_fp8_f32 v39, v28, v29 op_sel:[0,0,1]
	v_lshlrev_b64 v[24:25], 10, v[24:25]
	v_pk_add_f32 v[34:35], v[34:35], 1.0 op_sel_hi:[1,0]
	v_lshl_add_u64 v[24:25], s[46:47], 0, v[24:25]
	v_rcp_f32_e32 v34, v34
	v_rcp_f32_e32 v35, v35
	v_lshl_add_u64 v[24:25], v[24:25], 0, v[20:21]
	global_store_dwordx2 v[24:25], v[38:39], off
	v_pk_fma_f32 v[24:25], v[168:169], s[54:55], v[16:17] op_sel_hi:[1,0,1]
	v_pk_mul_f32 v[26:27], v[26:27], v[34:35]
	v_min_f32_e32 v24, 0x40e00000, v24
	v_min_f32_e32 v25, 0x40e00000, v25
	v_pk_mul_f32 v[34:35], v[24:25], s[56:57] op_sel_hi:[1,0]
	v_pk_fma_f32 v[36:37], v[134:135], s[54:55], v[2:3] op_sel_hi:[1,0,1]
	v_exp_f32_e32 v34, v34
	v_exp_f32_e32 v35, v35
	v_pk_fma_f32 v[30:31], v[162:163], s[54:55], v[10:11] op_sel_hi:[1,0,1]
	v_med3_f32 v36, v36, s85, v203
	v_med3_f32 v37, v37, s85, v203
	v_pk_add_f32 v[36:37], v[36:37], 1.0 op_sel_hi:[1,0]
	v_pk_add_f32 v[34:35], v[34:35], 1.0 op_sel_hi:[1,0]
	v_min_f32_e32 v30, 0x40e00000, v30
	v_min_f32_e32 v31, 0x40e00000, v31
	v_pk_mul_f32 v[26:27], v[36:37], v[26:27]
	v_rcp_f32_e32 v34, v34
	v_rcp_f32_e32 v35, v35
	v_pk_mul_f32 v[36:37], v[30:31], s[56:57] op_sel_hi:[1,0]
	v_pk_fma_f32 v[32:33], v[136:137], s[54:55], v[4:5] op_sel_hi:[1,0,1]
	v_exp_f32_e32 v36, v36
	v_exp_f32_e32 v37, v37
	v_med3_f32 v32, v32, s85, v203
	v_med3_f32 v33, v33, s85, v203
	v_pk_add_f32 v[32:33], v[32:33], 1.0 op_sel_hi:[1,0]
	v_pk_mul_f32 v[24:25], v[24:25], v[34:35]
	v_pk_fma_f32 v[28:29], v[164:165], s[54:55], v[12:13] op_sel_hi:[1,0,1]
	v_pk_mul_f32 v[24:25], v[32:33], v[24:25]
	v_pk_add_f32 v[32:33], v[36:37], 1.0 op_sel_hi:[1,0]
	v_min_f32_e32 v28, 0x40e00000, v28
	v_rcp_f32_e32 v32, v32
	v_rcp_f32_e32 v33, v33
	v_min_f32_e32 v29, 0x40e00000, v29
	v_or_b32_e32 v22, 48, v22
	v_ashrrev_i32_e32 v23, 31, v22
	v_pk_mul_f32 v[30:31], v[30:31], v[32:33]
	v_pk_mul_f32 v[32:33], v[28:29], s[56:57] op_sel_hi:[1,0]
	v_pk_fma_f32 v[40:41], v[130:131], s[54:55], v[6:7] op_sel_hi:[1,0,1]
	v_exp_f32_e32 v32, v32
	v_exp_f32_e32 v33, v33
	v_lshlrev_b64 v[22:23], 10, v[22:23]
	v_med3_f32 v34, v40, s85, v203
	v_med3_f32 v35, v41, s85, v203
	v_pk_add_f32 v[32:33], v[32:33], 1.0 op_sel_hi:[1,0]
	v_lshl_add_u64 v[22:23], s[46:47], 0, v[22:23]
	v_pk_add_f32 v[34:35], v[34:35], 1.0 op_sel_hi:[1,0]
	v_rcp_f32_e32 v32, v32
	v_rcp_f32_e32 v33, v33
	v_lshl_add_u64 v[20:21], v[22:23], 0, v[20:21]
	v_pk_fma_f32 v[22:23], v[126:127], s[54:55], v[14:15] op_sel_hi:[1,0,1]
	v_pk_mul_f32 v[30:31], v[34:35], v[30:31]
	v_mov_b32_e32 v36, 0
	v_mov_b32_e32 v37, 0
	v_min_f32_e32 v22, 0x40e00000, v22
	v_min_f32_e32 v23, 0x40e00000, v23
	v_pk_fma_f32 v[38:39], v[132:133], s[54:55], v[8:9] op_sel_hi:[1,0,1]
	v_cvt_pk_fp8_f32 v36, v26, v27
	v_cvt_pk_fp8_f32 v37, v30, v31
	v_pk_mul_f32 v[30:31], v[22:23], s[56:57] op_sel_hi:[1,0]
	v_med3_f32 v34, v38, s85, v203
	v_med3_f32 v35, v39, s85, v203
	v_exp_f32_e32 v30, v30
	v_exp_f32_e32 v31, v31
	v_pk_add_f32 v[34:35], v[34:35], 1.0 op_sel_hi:[1,0]
	v_pk_mul_f32 v[26:27], v[28:29], v[32:33]
	v_cvt_pk_fp8_f32 v36, v24, v25 op_sel:[0,0,1]
	v_pk_mul_f32 v[26:27], v[34:35], v[26:27]
	v_pk_add_f32 v[30:31], v[30:31], 1.0 op_sel_hi:[1,0]
	v_cvt_pk_fp8_f32 v37, v26, v27 op_sel:[0,0,1]
	v_rcp_f32_e32 v30, v30
	v_rcp_f32_e32 v31, v31
	v_pk_fma_f32 v[32:33], v[94:95], s[54:55], v[2:3] op_sel_hi:[1,0,1]
	global_store_dwordx2 v[20:21], v[36:37], off
	v_pk_fma_f32 v[20:21], v[128:129], s[54:55], v[16:17] op_sel_hi:[1,0,1]
	v_pk_mul_f32 v[22:23], v[22:23], v[30:31]
	v_min_f32_e32 v20, 0x40e00000, v20
	v_min_f32_e32 v21, 0x40e00000, v21
	v_pk_mul_f32 v[30:31], v[20:21], s[56:57] op_sel_hi:[1,0]
	v_pk_fma_f32 v[26:27], v[122:123], s[54:55], v[10:11] op_sel_hi:[1,0,1]
	v_exp_f32_e32 v30, v30
	v_exp_f32_e32 v31, v31
	v_med3_f32 v32, v32, s85, v203
	v_med3_f32 v33, v33, s85, v203
	v_pk_add_f32 v[32:33], v[32:33], 1.0 op_sel_hi:[1,0]
	v_pk_add_f32 v[30:31], v[30:31], 1.0 op_sel_hi:[1,0]
	v_min_f32_e32 v26, 0x40e00000, v26
	v_min_f32_e32 v27, 0x40e00000, v27
	v_pk_mul_f32 v[22:23], v[32:33], v[22:23]
	v_rcp_f32_e32 v30, v30
	v_rcp_f32_e32 v31, v31
	v_pk_mul_f32 v[32:33], v[26:27], s[56:57] op_sel_hi:[1,0]
	v_pk_fma_f32 v[28:29], v[96:97], s[54:55], v[4:5] op_sel_hi:[1,0,1]
	v_exp_f32_e32 v32, v32
	v_exp_f32_e32 v33, v33
	v_med3_f32 v28, v28, s85, v203
	v_med3_f32 v29, v29, s85, v203
	v_pk_add_f32 v[28:29], v[28:29], 1.0 op_sel_hi:[1,0]
	v_pk_mul_f32 v[20:21], v[20:21], v[30:31]
	v_pk_fma_f32 v[24:25], v[124:125], s[54:55], v[12:13] op_sel_hi:[1,0,1]
	v_pk_mul_f32 v[20:21], v[28:29], v[20:21]
	v_pk_add_f32 v[28:29], v[32:33], 1.0 op_sel_hi:[1,0]
	v_min_f32_e32 v24, 0x40e00000, v24
	v_rcp_f32_e32 v28, v28
	v_rcp_f32_e32 v29, v29
	v_min_f32_e32 v25, 0x40e00000, v25
	v_pk_fma_f32 v[36:37], v[90:91], s[54:55], v[6:7] op_sel_hi:[1,0,1]
	v_mov_b32_e32 v33, 0
	v_pk_mul_f32 v[26:27], v[26:27], v[28:29]
	v_pk_mul_f32 v[28:29], v[24:25], s[56:57] op_sel_hi:[1,0]
	v_med3_f32 v30, v36, s85, v203
	v_exp_f32_e32 v28, v28
	v_exp_f32_e32 v29, v29
	v_med3_f32 v31, v37, s85, v203
	v_pk_add_f32 v[30:31], v[30:31], 1.0 op_sel_hi:[1,0]
	v_pk_fma_f32 v[34:35], v[92:93], s[54:55], v[8:9] op_sel_hi:[1,0,1]
	v_pk_add_f32 v[28:29], v[28:29], 1.0 op_sel_hi:[1,0]
	v_pk_mul_f32 v[26:27], v[30:31], v[26:27]
	v_rcp_f32_e32 v28, v28
	v_rcp_f32_e32 v29, v29
	v_cvt_pk_fp8_f32 v33, v26, v27
	v_med3_f32 v30, v34, s85, v203
	v_med3_f32 v31, v35, s85, v203
	v_mov_b32_e32 v32, 0
	v_pk_add_f32 v[30:31], v[30:31], 1.0 op_sel_hi:[1,0]
	v_cvt_pk_fp8_f32 v32, v22, v23
	v_pk_mul_f32 v[22:23], v[24:25], v[28:29]
	v_pk_fma_f32 v[26:27], v[114:115], s[54:55], v[10:11] op_sel_hi:[1,0,1]
	v_pk_mul_f32 v[22:23], v[30:31], v[22:23]
	v_cvt_pk_fp8_f32 v32, v20, v21 op_sel:[0,0,1]
	v_cvt_pk_fp8_f32 v33, v22, v23 op_sel:[0,0,1]
	v_pk_fma_f32 v[22:23], v[118:119], s[54:55], v[14:15] op_sel_hi:[1,0,1]
	v_add_co_u32_e32 v20, vcc, s83, v18
	v_min_f32_e32 v22, 0x40e00000, v22
	v_min_f32_e32 v23, 0x40e00000, v23
	v_pk_mul_f32 v[30:31], v[22:23], s[56:57] op_sel_hi:[1,0]
	v_addc_co_u32_e32 v21, vcc, 0, v19, vcc
	v_exp_f32_e32 v30, v30
	v_exp_f32_e32 v31, v31
	global_store_dwordx2 v[20:21], v[32:33], off
	v_pk_fma_f32 v[20:21], v[120:121], s[54:55], v[16:17] op_sel_hi:[1,0,1]
	v_pk_fma_f32 v[32:33], v[86:87], s[54:55], v[2:3] op_sel_hi:[1,0,1]
	v_pk_add_f32 v[30:31], v[30:31], 1.0 op_sel_hi:[1,0]
	v_min_f32_e32 v20, 0x40e00000, v20
	v_rcp_f32_e32 v30, v30
	v_rcp_f32_e32 v31, v31
	v_min_f32_e32 v21, 0x40e00000, v21
	v_med3_f32 v32, v32, s85, v203
	v_med3_f32 v33, v33, s85, v203
	v_pk_mul_f32 v[22:23], v[22:23], v[30:31]
	v_pk_mul_f32 v[30:31], v[20:21], s[56:57] op_sel_hi:[1,0]
	v_pk_add_f32 v[32:33], v[32:33], 1.0 op_sel_hi:[1,0]
	v_exp_f32_e32 v30, v30
	v_exp_f32_e32 v31, v31
	v_min_f32_e32 v26, 0x40e00000, v26
	v_min_f32_e32 v27, 0x40e00000, v27
	v_pk_mul_f32 v[22:23], v[32:33], v[22:23]
	v_pk_add_f32 v[30:31], v[30:31], 1.0 op_sel_hi:[1,0]
	v_pk_mul_f32 v[32:33], v[26:27], s[56:57] op_sel_hi:[1,0]
	v_rcp_f32_e32 v30, v30
	v_rcp_f32_e32 v31, v31
	v_exp_f32_e32 v32, v32
	v_exp_f32_e32 v33, v33
	v_pk_fma_f32 v[28:29], v[88:89], s[54:55], v[4:5] op_sel_hi:[1,0,1]
	v_pk_mul_f32 v[20:21], v[20:21], v[30:31]
	v_med3_f32 v28, v28, s85, v203
	v_med3_f32 v29, v29, s85, v203
	v_pk_add_f32 v[28:29], v[28:29], 1.0 op_sel_hi:[1,0]
	v_pk_fma_f32 v[24:25], v[116:117], s[54:55], v[12:13] op_sel_hi:[1,0,1]
	v_pk_mul_f32 v[20:21], v[28:29], v[20:21]
	v_pk_add_f32 v[28:29], v[32:33], 1.0 op_sel_hi:[1,0]
	v_min_f32_e32 v24, 0x40e00000, v24
	v_rcp_f32_e32 v28, v28
	v_rcp_f32_e32 v29, v29
	v_min_f32_e32 v25, 0x40e00000, v25
	v_pk_fma_f32 v[36:37], v[82:83], s[54:55], v[6:7] op_sel_hi:[1,0,1]
	v_mov_b32_e32 v33, 0
	v_pk_mul_f32 v[26:27], v[26:27], v[28:29]
	v_pk_mul_f32 v[28:29], v[24:25], s[56:57] op_sel_hi:[1,0]
	v_med3_f32 v30, v36, s85, v203
	v_exp_f32_e32 v28, v28
	v_exp_f32_e32 v29, v29
	v_med3_f32 v31, v37, s85, v203
	v_pk_add_f32 v[30:31], v[30:31], 1.0 op_sel_hi:[1,0]
	v_pk_fma_f32 v[34:35], v[84:85], s[54:55], v[8:9] op_sel_hi:[1,0,1]
	v_pk_add_f32 v[28:29], v[28:29], 1.0 op_sel_hi:[1,0]
	v_pk_mul_f32 v[26:27], v[30:31], v[26:27]
	v_rcp_f32_e32 v28, v28
	v_rcp_f32_e32 v29, v29
	v_cvt_pk_fp8_f32 v33, v26, v27
	v_med3_f32 v30, v34, s85, v203
	v_med3_f32 v31, v35, s85, v203
	v_mov_b32_e32 v32, 0
	v_pk_add_f32 v[30:31], v[30:31], 1.0 op_sel_hi:[1,0]
	v_cvt_pk_fp8_f32 v32, v22, v23
	v_pk_mul_f32 v[22:23], v[24:25], v[28:29]
	v_pk_fma_f32 v[26:27], v[106:107], s[54:55], v[10:11] op_sel_hi:[1,0,1]
	v_pk_mul_f32 v[22:23], v[30:31], v[22:23]
	v_cvt_pk_fp8_f32 v32, v20, v21 op_sel:[0,0,1]
	v_cvt_pk_fp8_f32 v33, v22, v23 op_sel:[0,0,1]
	v_pk_fma_f32 v[22:23], v[110:111], s[54:55], v[14:15] op_sel_hi:[1,0,1]
	v_add_co_u32_e32 v20, vcc, s86, v18
	v_min_f32_e32 v22, 0x40e00000, v22
	v_min_f32_e32 v23, 0x40e00000, v23
	v_pk_mul_f32 v[30:31], v[22:23], s[56:57] op_sel_hi:[1,0]
	v_addc_co_u32_e32 v21, vcc, 0, v19, vcc
	v_exp_f32_e32 v30, v30
	v_exp_f32_e32 v31, v31
	global_store_dwordx2 v[20:21], v[32:33], off
	v_pk_fma_f32 v[20:21], v[112:113], s[54:55], v[16:17] op_sel_hi:[1,0,1]
	v_pk_fma_f32 v[32:33], v[78:79], s[54:55], v[2:3] op_sel_hi:[1,0,1]
	v_pk_add_f32 v[30:31], v[30:31], 1.0 op_sel_hi:[1,0]
	v_min_f32_e32 v20, 0x40e00000, v20
	v_rcp_f32_e32 v30, v30
	v_rcp_f32_e32 v31, v31
	v_min_f32_e32 v21, 0x40e00000, v21
	v_med3_f32 v32, v32, s85, v203
	v_med3_f32 v33, v33, s85, v203
	v_pk_mul_f32 v[22:23], v[22:23], v[30:31]
	v_pk_mul_f32 v[30:31], v[20:21], s[56:57] op_sel_hi:[1,0]
	v_pk_add_f32 v[32:33], v[32:33], 1.0 op_sel_hi:[1,0]
	v_exp_f32_e32 v30, v30
	v_exp_f32_e32 v31, v31
	v_min_f32_e32 v26, 0x40e00000, v26
	v_min_f32_e32 v27, 0x40e00000, v27
	v_pk_mul_f32 v[22:23], v[32:33], v[22:23]
	v_pk_add_f32 v[30:31], v[30:31], 1.0 op_sel_hi:[1,0]
	v_pk_mul_f32 v[32:33], v[26:27], s[56:57] op_sel_hi:[1,0]
	v_rcp_f32_e32 v30, v30
	v_rcp_f32_e32 v31, v31
	v_exp_f32_e32 v32, v32
	v_exp_f32_e32 v33, v33
	v_pk_fma_f32 v[28:29], v[80:81], s[54:55], v[4:5] op_sel_hi:[1,0,1]
	v_pk_mul_f32 v[20:21], v[20:21], v[30:31]
	v_med3_f32 v28, v28, s85, v203
	v_med3_f32 v29, v29, s85, v203
	v_pk_add_f32 v[28:29], v[28:29], 1.0 op_sel_hi:[1,0]
	v_pk_fma_f32 v[24:25], v[108:109], s[54:55], v[12:13] op_sel_hi:[1,0,1]
	v_pk_mul_f32 v[20:21], v[28:29], v[20:21]
	v_pk_add_f32 v[28:29], v[32:33], 1.0 op_sel_hi:[1,0]
	v_min_f32_e32 v24, 0x40e00000, v24
	v_rcp_f32_e32 v28, v28
	v_rcp_f32_e32 v29, v29
	v_min_f32_e32 v25, 0x40e00000, v25
	v_pk_fma_f32 v[36:37], v[74:75], s[54:55], v[6:7] op_sel_hi:[1,0,1]
	v_mov_b32_e32 v32, 0
	v_pk_mul_f32 v[26:27], v[26:27], v[28:29]
	v_pk_mul_f32 v[28:29], v[24:25], s[56:57] op_sel_hi:[1,0]
	v_med3_f32 v30, v36, s85, v203
	v_exp_f32_e32 v28, v28
	v_exp_f32_e32 v29, v29
	v_med3_f32 v31, v37, s85, v203
	v_pk_add_f32 v[30:31], v[30:31], 1.0 op_sel_hi:[1,0]
	v_mov_b32_e32 v33, 0
	v_pk_add_f32 v[28:29], v[28:29], 1.0 op_sel_hi:[1,0]
	v_pk_mul_f32 v[26:27], v[30:31], v[26:27]
	v_rcp_f32_e32 v28, v28
	v_rcp_f32_e32 v29, v29
	v_pk_fma_f32 v[34:35], v[76:77], s[54:55], v[8:9] op_sel_hi:[1,0,1]
	v_cvt_pk_fp8_f32 v32, v22, v23
	v_cvt_pk_fp8_f32 v33, v26, v27
	v_med3_f32 v30, v34, s85, v203
	v_med3_f32 v31, v35, s85, v203
	v_pk_add_f32 v[30:31], v[30:31], 1.0 op_sel_hi:[1,0]
	v_pk_mul_f32 v[22:23], v[24:25], v[28:29]
	v_cvt_pk_fp8_f32 v32, v20, v21 op_sel:[0,0,1]
	v_pk_mul_f32 v[22:23], v[30:31], v[22:23]
	v_add_co_u32_e32 v20, vcc, s87, v18
	v_cvt_pk_fp8_f32 v33, v22, v23 op_sel:[0,0,1]
	v_pk_fma_f32 v[14:15], v[102:103], s[54:55], v[14:15] op_sel_hi:[1,0,1]
	v_addc_co_u32_e32 v21, vcc, 0, v19, vcc
	v_min_f32_e32 v14, 0x40e00000, v14
	v_min_f32_e32 v15, 0x40e00000, v15
	global_store_dwordx2 v[20:21], v[32:33], off
	v_pk_mul_f32 v[20:21], v[14:15], s[56:57] op_sel_hi:[1,0]
	v_pk_fma_f32 v[16:17], v[104:105], s[54:55], v[16:17] op_sel_hi:[1,0,1]
	v_exp_f32_e32 v20, v20
	v_exp_f32_e32 v21, v21
	v_min_f32_e32 v16, 0x40e00000, v16
	v_min_f32_e32 v17, 0x40e00000, v17
	v_pk_fma_f32 v[2:3], v[70:71], s[54:55], v[2:3] op_sel_hi:[1,0,1]
	v_pk_add_f32 v[20:21], v[20:21], 1.0 op_sel_hi:[1,0]
	v_med3_f32 v2, v2, s85, v203
	v_rcp_f32_e32 v20, v20
	v_rcp_f32_e32 v21, v21
	v_med3_f32 v3, v3, s85, v203
	v_pk_fma_f32 v[10:11], v[98:99], s[54:55], v[10:11] op_sel_hi:[1,0,1]
	v_pk_add_f32 v[2:3], v[2:3], 1.0 op_sel_hi:[1,0]
	v_pk_mul_f32 v[14:15], v[14:15], v[20:21]
	v_pk_mul_f32 v[20:21], v[16:17], s[56:57] op_sel_hi:[1,0]
	v_pk_mul_f32 v[2:3], v[2:3], v[14:15]
	v_exp_f32_e32 v20, v20
	v_exp_f32_e32 v21, v21
	v_min_f32_e32 v10, 0x40e00000, v10
	v_min_f32_e32 v11, 0x40e00000, v11
	v_pk_fma_f32 v[4:5], v[72:73], s[54:55], v[4:5] op_sel_hi:[1,0,1]
	v_pk_add_f32 v[14:15], v[20:21], 1.0 op_sel_hi:[1,0]
	v_pk_mul_f32 v[20:21], v[10:11], s[56:57] op_sel_hi:[1,0]
	v_rcp_f32_e32 v14, v14
	v_rcp_f32_e32 v15, v15
	v_exp_f32_e32 v20, v20
	v_exp_f32_e32 v21, v21
	v_med3_f32 v4, v4, s85, v203
	v_med3_f32 v5, v5, s85, v203
	v_pk_add_f32 v[4:5], v[4:5], 1.0 op_sel_hi:[1,0]
	v_pk_mul_f32 v[14:15], v[16:17], v[14:15]
	v_pk_fma_f32 v[12:13], v[100:101], s[54:55], v[12:13] op_sel_hi:[1,0,1]
	v_pk_mul_f32 v[4:5], v[4:5], v[14:15]
	v_pk_add_f32 v[14:15], v[20:21], 1.0 op_sel_hi:[1,0]
	v_min_f32_e32 v12, 0x40e00000, v12
	v_rcp_f32_e32 v14, v14
	v_rcp_f32_e32 v15, v15
	v_min_f32_e32 v13, 0x40e00000, v13
	v_pk_fma_f32 v[6:7], v[66:67], s[54:55], v[6:7] op_sel_hi:[1,0,1]
	v_pk_fma_f32 v[8:9], v[68:69], s[54:55], v[8:9] op_sel_hi:[1,0,1]
	v_pk_mul_f32 v[10:11], v[10:11], v[14:15]
	v_pk_mul_f32 v[14:15], v[12:13], s[56:57] op_sel_hi:[1,0]
	v_med3_f32 v6, v6, s85, v203
	v_exp_f32_e32 v14, v14
	v_exp_f32_e32 v15, v15
	v_med3_f32 v7, v7, s85, v203
	v_pk_add_f32 v[6:7], v[6:7], 1.0 op_sel_hi:[1,0]
	v_med3_f32 v8, v8, s85, v203
	v_pk_mul_f32 v[6:7], v[6:7], v[10:11]
	v_pk_add_f32 v[10:11], v[14:15], 1.0 op_sel_hi:[1,0]
	v_mov_b32_e32 v14, 0
	v_rcp_f32_e32 v10, v10
	v_rcp_f32_e32 v11, v11
	v_mov_b32_e32 v15, 0
	v_cvt_pk_fp8_f32 v14, v2, v3
	v_cvt_pk_fp8_f32 v15, v6, v7
	v_med3_f32 v9, v9, s85, v203
	v_pk_add_f32 v[8:9], v[8:9], 1.0 op_sel_hi:[1,0]
	v_pk_mul_f32 v[2:3], v[12:13], v[10:11]
	v_cvt_pk_fp8_f32 v14, v4, v5 op_sel:[0,0,1]
	v_pk_mul_f32 v[2:3], v[8:9], v[2:3]
	v_mov_b32_e32 v5, v214
	v_cvt_pk_fp8_f32 v15, v2, v3 op_sel:[0,0,1]
	v_add_co_u32_e32 v2, vcc, 0x2c000, v18
	v_mov_b32_e32 v4, v212
	s_nop 0
	v_addc_co_u32_e32 v3, vcc, 0, v19, vcc
	global_store_dwordx2 v[2:3], v[14:15], off
	s_and_b64 vcc, exec, s[4:5]
	v_mov_b32_e32 v2, v213
	v_mov_b32_e32 v3, v211
	s_cbranch_vccnz .LBB0_718
	v_mov_b32_e32 v2, v194
	s_nop 0
	v_ashrrev_i32_e32 v3, 31, v2
	v_lshrrev_b32_e32 v3, 26, v3
	v_lshlrev_b32_e32 v4, 4, v2
	v_add_u32_e32 v3, v2, v3
	v_bfe_i32 v2, v2, 27, 1
	v_lshrrev_b32_e32 v2, 22, v2
	v_add_u32_e32 v2, v4, v2
	v_and_b32_e32 v2, 0xfffffc00, v2
	v_sub_u32_e32 v2, v4, v2
	v_lshrrev_b32_e32 v5, 4, v2
	v_bitop3_b32 v5, v5, v2, 32 bitop3:0x6c
	v_ashrrev_i32_e32 v2, 31, v2
	v_lshrrev_b32_e32 v2, 26, v2
	v_add_u32_e32 v2, v5, v2
	v_and_b32_e32 v2, 0xc0, v2
	v_add_u32_e32 v4, 0x2000, v4
	v_sub_u32_e32 v2, v5, v2
	v_ashrrev_i32_e32 v5, 31, v4
	v_lshrrev_b32_e32 v5, 22, v5
	v_add_u32_e32 v5, v4, v5
	v_ashrrev_i32_e32 v5, 10, v5
	v_mul_i32_i24_e32 v6, 0x400, v5
	v_sub_u32_e32 v4, v4, v6
	v_lshrrev_b32_e32 v6, 4, v4
	v_bitop3_b32 v6, v6, v4, 32 bitop3:0x6c
	v_ashrrev_i32_e32 v4, 31, v4
	v_lshrrev_b32_e32 v4, 26, v4
	v_add_u32_e32 v4, v6, v4
	v_and_b32_e32 v4, 0xc0, v4
	v_sub_u32_e32 v4, v6, v4
	v_lshrrev_b32_e32 v3, 1, v3
	v_ashrrev_i16_sdwa v2, v195, sext(v2) dst_sel:DWORD dst_unused:UNUSED_PAD src0_sel:DWORD src1_sel:BYTE_0
	v_lshlrev_b32_e32 v5, 5, v5
	v_ashrrev_i16_sdwa v4, v195, sext(v4) dst_sel:DWORD dst_unused:UNUSED_PAD src0_sel:DWORD src1_sel:BYTE_0
	v_and_b32_e32 v3, 32, v3
	v_bfe_i32 v2, v2, 0, 16
	v_and_b32_e32 v5, 32, v5
	v_bfe_i32 v4, v4, 0, 16
	v_add_lshl_u32 v2, v3, v2, 1
	v_add_lshl_u32 v5, v5, v4, 1
	v_lshl_add_u32 v3, v205, 10, v2
	v_lshl_add_u32 v2, v204, 10, v2
	v_lshl_add_u32 v4, v209, 10, v5
	v_lshl_add_u32 v5, v207, 10, v5
